# K: MoE-down: bias folded into accumulator init with next-unit bias prefetch (same scheme as MoE-up)
# speedup vs baseline: 1.0080x; 1.0003x over previous
; #define PG8_WAIT_V(n) asm volatile("s_waitcnt vmcnt(" #n ")" ::: "memory")
; template <class Epi, class Sched, bool ALIGN_EPI = false, bool SP2 = false, bool GATHER = false, bool HALFM = false>
; __device__ __forceinline__ void gemm_phase(PG8_LAS unsigned char* lds, const int Kdim, const Sched& S, const Epi& E) {
;     ...
;     Unit cur, nxt; int ui = 0;
;     if (!S.next(0, cur)) return;
;     f32x4 acc[2][2][4][2];
; #pragma unroll
;     for (int a = 0; a < 2; ++a)
; #pragma unroll
;         for (int b = 0; b < 2; ++b)
; #pragma unroll
;             for (int m = 0; m < 4; ++m)
; #pragma unroll
;                 for (int n = 0; n < 2; ++n) acc[a][b][m][n] = (f32x4){0.f, 0.f, 0.f, 0.f};
;     bf16x8 At[4][2], B0[2][2], B1[2][2];
;     const char* cA = cur.a; const char* cB = cur.b;
;     S.a_ready(cur);
;     const char* gA = nullptr; unsigned gc[2][2] = {{0u, 0u}, {0u, 0u}}, gn[2][2] = {{0u, 0u}, {0u, 0u}};
;     if constexpr (GATHER) { static_assert(SP2, "GATHER needs the SP2 loop"); gA = S.abase();
;         Unit u1; const bool h1 = S.next(1, u1);
; #pragma unroll
;         for (int h = 0; h < 2; ++h)
; #pragma unroll
;             for (int i = 0; i < 2; ++i) { gc[h][i] = (unsigned)S.row_index(cur, h * HALF + RA[i]) * (unsigned)(K * 2) + CA2[i]; gn[h][i] = h1 ? (unsigned)S.row_index(u1, h * HALF + RA[i]) * (unsigned)(K * 2) + CA2[i] : gc[h][i]; } }
;     if constexpr (SP2) {
;         PG8_STAGE(PG8_SB(0, 0), cB, voffB); PG8_STAGE(PG8_SB(0, 1), cB + hstep, voffB);
;         if constexpr (GATHER) { PG8_STAGE_G(PG8_SA(0, 0), 0, gc[0]); PG8_STAGE_G(PG8_SA(0, 1), 0, gc[1]); } else { PG8_STAGE(PG8_SA(0, 0), cA, voffA); PG8_STAGE(PG8_SA(0, 1), cA + hstep, voffA); }
;         if (wr == 1) PG8_BAR;
;         PG8_WAIT_V(2); PG8_BAR;
;         PG8_STAGE(PG8_SB(1, 0), cB + kstep, voffB); if constexpr (GATHER) PG8_STAGE_G(PG8_SA(1, 0), kstep, gc[0]); else PG8_STAGE(PG8_SA(1, 0), cA + kstep, voffA); PG8_STAGE(PG8_SB(1, 1), cB + hstep + kstep, voffB);
;         PG8_WAIT_V(6); PG8_BAR;
;     __device__ __forceinline__ void operator()(const pg8::f32x4 (&acc)[2][2][4][2], const pg8::Unit& u, int wr, int wc, int fr, int fq) const {
;     ...
;         f32x4 bv[2][2];
; #pragma unroll
;         for (int bj = 0; bj < 2; ++bj)
; #pragma unroll
;             for (int n = 0; n < 2; ++n) bv[bj][n] = *(const f32x4*)(b_down + u.e * 1024 + col0 + bj * 128 + 4 * n);
.LBB0_1810:
	v_readlane_b32 s20, v255, 8
	v_readlane_b32 s21, v255, 9
	v_readlane_b32 s56, v251, 31
	s_lshl_b64 s[20:21], s[20:21], 17
	v_readlane_b32 s64, v251, 39
	v_bfe_u32 v20, v18, 4, 2
	v_readlane_b32 s65, v251, 40
	s_add_u32 s27, s64, s20
	v_and_b32_e32 v19, 15, v18
	v_lshlrev_b32_e32 v21, 3, v20
	v_lshlrev_b32_e32 v20, 4, v20
	v_lshlrev_b32_e32 v18, 2, v18
	s_addc_u32 s37, s65, s21
	s_and_b32 s20, s16, 3
	v_lshl_or_b32 v1, s15, 6, v19
	v_lshl_or_b32 v19, v19, 6, v20
	s_lshl_b32 s15, s15, 13
	v_and_b32_e32 v18, 32, v18
	s_add_i32 m0, s7, 0x18000
	v_lshl_add_u64 v[10:11], v[10:11], 0, s[34:35]
	v_bitop3_b32 v20, v19, s15, v18 bitop3:0xde
	s_lshl_b32 s15, s20, 12
	s_waitcnt vmcnt(2)
	s_barrier
	global_load_lds_dwordx4 v[10:11], off
	v_lshl_add_u64 v[8:9], v[8:9], 0, s[34:35]
	s_add_i32 m0, s7, 0x1a000
	s_add_i32 s46, s7, 0x8000
	s_add_i32 s47, s7, 0xa000
	global_load_lds_dwordx4 v[8:9], off
	v_lshl_add_u64 v[4:5], v[4:5], 0, s[34:35]
	s_mov_b32 m0, s46
	s_add_u32 s16, s24, 0x40080
	global_load_lds_dwordx4 v[4:5], off
	v_lshl_add_u64 v[4:5], v[6:7], 0, s[34:35]
	s_mov_b32 m0, s47
	s_addc_u32 s17, s25, 0
	global_load_lds_dwordx4 v[4:5], off
	s_add_i32 m0, s7, 0x1c000
	v_lshl_add_u64 v[4:5], s[16:17], 0, v[2:3]
	global_load_lds_dwordx4 v[4:5], off
	v_lshl_add_u64 v[4:5], s[16:17], 0, v[148:149]
	s_add_i32 m0, s7, 0x1e000
	s_cmpk_lt_u32 s14, 0x100
	global_load_lds_dwordx4 v[4:5], off
	v_lshlrev_b32_e32 v4, 14, v16
	v_and_b32_e32 v4, 0xffff8000, v4
	v_lshl_add_u32 v4, v15, 11, v4
	v_and_b32_e32 v5, 1, v16
	v_lshl_or_b32 v4, v5, 6, v4
	v_lshl_add_u32 v154, v17, 1, v4
	v_lshlrev_b32_e32 v4, 14, v12
	v_and_b32_e32 v4, 0xffff8000, v4
	s_waitcnt vmcnt(6)
	v_lshl_add_u32 v4, v13, 11, v4
	v_and_b32_e32 v5, 1, v12
	v_lshl_or_b32 v4, v5, 6, v4
	v_bitop3_b32 v160, v19, s15, v18 bitop3:0xde
	v_lshl_or_b32 v161, s20, 5, v21
	s_cselect_b64 s[14:15], -1, 0
	v_or_b32_e32 v162, 16, v1
	v_or_b32_e32 v163, 32, v1
	v_or_b32_e32 v164, 48, v1
	v_add_u32_e32 v165, 0x80, v1
	v_add_u32_e32 v166, 0x90, v1
	v_add_u32_e32 v167, 0xa0, v1
	v_add_u32_e32 v168, 0xb0, v1
	v_mov_b32_e32 v155, v3
	v_lshl_add_u32 v156, v14, 1, v4
	v_mov_b32_e32 v157, v3
	s_mov_b32 s48, 0
	v_add_u32_e32 v169, 0, v20
	v_readlane_b32 s57, v251, 32
	v_readlane_b32 s58, v251, 33
	v_readlane_b32 s59, v251, 34
	v_readlane_b32 s60, v251, 35
	v_readlane_b32 s61, v251, 36
	v_readlane_b32 s62, v251, 37
	v_readlane_b32 s63, v251, 38
	v_readlane_b32 s66, v251, 41
	v_readlane_b32 s67, v251, 42
	v_readlane_b32 s68, v251, 43
	v_readlane_b32 s69, v251, 44
	v_readlane_b32 s70, v251, 45
	v_readlane_b32 s71, v251, 46
	s_barrier
	s_lshl_b32 s20, s51, 10
	s_ashr_i32 s21, s20, 31
	s_lshl_b64 s[20:21], s[20:21], 2
	v_lshl_or_b32 v104, s52, 8, v161
	s_add_u32 s20, s27, s20
	s_addc_u32 s21, s37, s21
	v_ashrrev_i32_e32 v105, 31, v104
	v_lshl_add_u64 v[104:105], v[104:105], 2, s[20:21]
	global_load_dwordx4 v[186:189], v[104:105], off
	global_load_dwordx4 v[190:193], v[104:105], off offset:16
	global_load_dwordx4 v[194:197], v[104:105], off offset:512
	global_load_dwordx4 v[198:201], v[104:105], off offset:528
	s_waitcnt vmcnt(0)
	s_branch .LBB0_1813

; #define PG8_BAR __builtin_amdgcn_s_barrier()
; template <class Epi, class Sched, bool ALIGN_EPI = false, bool SP2 = false, bool GATHER = false, bool HALFM = false>
; __device__ __forceinline__ void gemm_phase(PG8_LAS unsigned char* lds, const int Kdim, const Sched& S, const Epi& E) {
;     ...
;     f32x4 acc[2][2][4][2];
; #pragma unroll
;     for (int a = 0; a < 2; ++a)
; #pragma unroll
;         for (int b = 0; b < 2; ++b)
; #pragma unroll
;             for (int m = 0; m < 4; ++m)
; #pragma unroll
;                 for (int n = 0; n < 2; ++n) acc[a][b][m][n] = (f32x4){0.f, 0.f, 0.f, 0.f};
;     ...
; #pragma unroll
;         for (int a = 0; a < 2; ++a)
; #pragma unroll
;             for (int b = 0; b < 2; ++b)
; #pragma unroll
;                 for (int m = 0; m < 4; ++m)
; #pragma unroll
;                     for (int n = 0; n < 2; ++n) acc[a][b][m][n] = (f32x4){0.f, 0.f, 0.f, 0.f};
;         cur = nxt; cA = nA; cB = nB; ++ui;
;         if constexpr (GATHER) {
; #pragma unroll
;             for (int h = 0; h < 2; ++h)
; #pragma unroll
;                 for (int i = 0; i < 2; ++i) { gc[h][i] = gn[h][i]; if (has_nn) gn[h][i] = (unsigned)ix[h][i] * (unsigned)(K * 2) + CA2[i]; } }
;         if constexpr (ALIGN_EPI) { if (wr == 1) PG8_BAR; }
.LBB0_1816:
	s_and_b64 s[20:21], s[42:43], exec
	s_cselect_b32 s17, s39, s5
	s_cselect_b32 s36, s38, s4
	s_cselect_b32 s53, s41, s25
	s_cselect_b32 s54, s40, s24
	s_add_u32 s44, s4, 0x40080
	s_addc_u32 s45, s5, 0
	s_add_u32 s55, s24, 0x100
	s_waitcnt vmcnt(16)
	v_mov_b32_e32 v4, v198
	s_addc_u32 s56, s25, 0
	s_mov_b32 s57, -2
	v_mov_b32_e32 v5, v199
	v_mov_b32_e32 v6, v200
	v_mov_b32_e32 v7, v201
	v_mov_b32_e32 v8, v194
	v_mov_b32_e32 v9, v195
	v_mov_b32_e32 v10, v196
	v_mov_b32_e32 v11, v197
	v_mov_b32_e32 v16, v198
	v_mov_b32_e32 v17, v199
	v_mov_b32_e32 v18, v200
	v_mov_b32_e32 v19, v201
	v_mov_b32_e32 v24, v194
	v_mov_b32_e32 v25, v195
	v_mov_b32_e32 v26, v196
	v_mov_b32_e32 v27, v197
	v_mov_b32_e32 v32, v198
	v_mov_b32_e32 v33, v199
	v_mov_b32_e32 v34, v200
	v_mov_b32_e32 v35, v201
	v_mov_b32_e32 v40, v194
	v_mov_b32_e32 v41, v195
	v_mov_b32_e32 v42, v196
	v_mov_b32_e32 v43, v197
	v_mov_b32_e32 v48, v198
	v_mov_b32_e32 v49, v199
	v_mov_b32_e32 v50, v200
	v_mov_b32_e32 v51, v201
	v_mov_b32_e32 v56, v194
	v_mov_b32_e32 v57, v195
	v_mov_b32_e32 v58, v196
	v_mov_b32_e32 v59, v197
	v_mov_b32_e32 v12, v190
	v_mov_b32_e32 v13, v191
	v_mov_b32_e32 v14, v192
	v_mov_b32_e32 v15, v193
	v_mov_b32_e32 v20, v186
	v_mov_b32_e32 v21, v187
	v_mov_b32_e32 v22, v188
	v_mov_b32_e32 v23, v189
	v_mov_b32_e32 v28, v190
	v_mov_b32_e32 v29, v191
	v_mov_b32_e32 v30, v192
	v_mov_b32_e32 v31, v193
	v_mov_b32_e32 v36, v186
	v_mov_b32_e32 v37, v187
	v_mov_b32_e32 v38, v188
	v_mov_b32_e32 v39, v189
	v_mov_b32_e32 v44, v190
	v_mov_b32_e32 v45, v191
	v_mov_b32_e32 v46, v192
	v_mov_b32_e32 v47, v193
	v_mov_b32_e32 v52, v186
	v_mov_b32_e32 v53, v187
	v_mov_b32_e32 v54, v188
	v_mov_b32_e32 v55, v189
	v_mov_b32_e32 v60, v190
	v_mov_b32_e32 v61, v191
	v_mov_b32_e32 v62, v192
	v_mov_b32_e32 v63, v193
	v_mov_b32_e32 v64, v186
	v_mov_b32_e32 v65, v187
	v_mov_b32_e32 v66, v188
	v_mov_b32_e32 v67, v189
	v_mov_b32_e32 v68, v198
	v_mov_b32_e32 v69, v199
	v_mov_b32_e32 v70, v200
	v_mov_b32_e32 v71, v201
	v_mov_b32_e32 v72, v194
	v_mov_b32_e32 v73, v195
	v_mov_b32_e32 v74, v196
	v_mov_b32_e32 v75, v197
	v_mov_b32_e32 v84, v198
	v_mov_b32_e32 v85, v199
	v_mov_b32_e32 v86, v200
	v_mov_b32_e32 v87, v201
	v_mov_b32_e32 v88, v194
	v_mov_b32_e32 v89, v195
	v_mov_b32_e32 v90, v196
	v_mov_b32_e32 v91, v197
	v_mov_b32_e32 v116, v198
	v_mov_b32_e32 v117, v199
	v_mov_b32_e32 v118, v200
	v_mov_b32_e32 v119, v201
	v_mov_b32_e32 v120, v194
	v_mov_b32_e32 v121, v195
	v_mov_b32_e32 v122, v196
	v_mov_b32_e32 v123, v197
	v_mov_b32_e32 v132, v198
	v_mov_b32_e32 v133, v199
	v_mov_b32_e32 v134, v200
	v_mov_b32_e32 v135, v201
	v_mov_b32_e32 v136, v194
	v_mov_b32_e32 v137, v195
	v_mov_b32_e32 v138, v196
	v_mov_b32_e32 v139, v197
	v_mov_b32_e32 v76, v190
	v_mov_b32_e32 v77, v191
	v_mov_b32_e32 v78, v192
	v_mov_b32_e32 v79, v193
	v_mov_b32_e32 v80, v186
	v_mov_b32_e32 v81, v187
	v_mov_b32_e32 v82, v188
	v_mov_b32_e32 v83, v189
	v_mov_b32_e32 v92, v190
	v_mov_b32_e32 v93, v191
	v_mov_b32_e32 v94, v192
	v_mov_b32_e32 v95, v193
	v_mov_b32_e32 v96, v186
	v_mov_b32_e32 v97, v187
	v_mov_b32_e32 v98, v188
	v_mov_b32_e32 v99, v189
	v_mov_b32_e32 v124, v190
	v_mov_b32_e32 v125, v191
	v_mov_b32_e32 v126, v192
	v_mov_b32_e32 v127, v193
	v_mov_b32_e32 v128, v186
	v_mov_b32_e32 v129, v187
	v_mov_b32_e32 v130, v188
	v_mov_b32_e32 v131, v189
	v_mov_b32_e32 v140, v190
	v_mov_b32_e32 v141, v191
	v_mov_b32_e32 v142, v192
	v_mov_b32_e32 v143, v193
	v_mov_b32_e32 v144, v186
	v_mov_b32_e32 v145, v187
	v_mov_b32_e32 v146, v188
	v_mov_b32_e32 v147, v189
	s_cmp_eq_u32 s48, 1
	s_cbranch_scc1 .Ldn_unit_nobar
	s_cmp_eq_u64 s[0:1], 0
	s_cbranch_scc1 .Ldn_unit_nobar
	s_barrier

; template <class Epi, class Sched, bool ALIGN_EPI = false, bool SP2 = false, bool GATHER = false, bool HALFM = false>
; __device__ __forceinline__ void gemm_phase(PG8_LAS unsigned char* lds, const int Kdim, const Sched& S, const Epi& E) {
;     ...
;         if (!has_next) break;
;     __device__ __forceinline__ void operator()(const pg8::f32x4 (&acc)[2][2][4][2], const pg8::Unit& u, int wr, int wc, int fr, int fq) const {
;         const bool side = side_layer >= 0 && u.lx < 1152; const int sit = 18432 + u.lx * 8 + wr * 4 + wc, slane = fq * 16 + fr;
;         f32x4 sv[8];
;         if (side) moe_item_load(*sp, side_layer, sit, slane, sv);
;         const int col0 = u.pn * 256 + wc * 32 + 8 * fq;
;         f32x4 bv[2][2];
; #pragma unroll
;         for (int bj = 0; bj < 2; ++bj)
; #pragma unroll
;             for (int n = 0; n < 2; ++n) bv[bj][n] = *(const f32x4*)(b_down + u.e * 1024 + col0 + bj * 128 + 4 * n);
.LBB0_1820:
	v_lshl_or_b32 v158, s52, 8, v161
	v_ashrrev_i32_e32 v159, 31, v158
	v_add_u32_e32 v170, s6, v1
	v_ashrrev_i32_e32 v171, 31, v170
	v_lshlrev_b64 v[170:171], 11, v[170:171]
	v_lshl_add_u64 v[170:171], s[10:11], 0, v[170:171]
	v_lshlrev_b64 v[158:159], 1, v[158:159]
	v_lshl_add_u64 v[170:171], v[170:171], 0, v[158:159]
	v_readlane_b32 s76, v255, 5
	v_readlane_b32 s77, v255, 6
	s_movk_i32 s33, 0x1dff
	s_and_b64 vcc, exec, s[42:43]
	s_cbranch_vccz .Ldn_epi_nonext
	s_lshl_b32 s4, s49, 10
	s_ashr_i32 s5, s4, 31
	s_lshl_b64 s[4:5], s[4:5], 2
	v_lshl_or_b32 v104, s50, 8, v161
	s_add_u32 s4, s27, s4
	s_addc_u32 s5, s37, s5
	v_ashrrev_i32_e32 v105, 31, v104
	v_lshl_add_u64 v[104:105], v[104:105], 2, s[4:5]
	global_load_dwordx4 v[186:189], v[104:105], off
	global_load_dwordx4 v[190:193], v[104:105], off offset:16
	global_load_dwordx4 v[194:197], v[104:105], off offset:512
	global_load_dwordx4 v[198:201], v[104:105], off offset:528
; __device__ __forceinline__ unsigned cvt_pk_bf16(float lo, float hi) { unsigned r; asm volatile("v_cvt_pk_bf16_f32 %0, %1, %2" : "=v"(r) : "v"(lo), "v"(hi)); return r; }
;     __device__ __forceinline__ void operator()(const pg8::f32x4 (&acc)[2][2][4][2], const pg8::Unit& u, int wr, int wc, int fr, int fq) const {
;     ...
; #pragma unroll
;         for (int ai = 0; ai < 2; ++ai)
; #pragma unroll
;             for (int m = 0; m < 4; ++m) {
;                 bf16_t* rowp = YS + (size_t)(u.pm + ai * 128 + wr * 64 + m * 16 + fr) * 1024 + col0;
; #pragma unroll
;                 for (int bj = 0; bj < 2; ++bj) {
;                     const f32x4 v0 = acc[ai][bj][m][0] + bv[bj][0], v1 = acc[ai][bj][m][1] + bv[bj][1];
;                     pg8::u32x4 w; w.x = pg8::cvt_pk_bf16(v0[0], v0[1]); w.y = pg8::cvt_pk_bf16(v0[2], v0[3]); w.z = pg8::cvt_pk_bf16(v1[0], v1[1]); w.w = pg8::cvt_pk_bf16(v1[2], v1[3]);
;                     *(pg8::u32x4*)(rowp + bj * 128) = w;
;                 }
;             }
.Ldn_epi_nonext:
	s_mov_b64 s[4:5], -1
	s_andn2_b64 vcc, exec, s[42:43]
	v_mov_b32_e32 v172, v142
	v_mov_b32_e32 v173, v143
	v_mov_b32_e32 v142, v140
	v_mov_b32_e32 v143, v141
	v_cvt_pk_bf16_f32 v140, v144, v145
	v_cvt_pk_bf16_f32 v141, v146, v147
	v_cvt_pk_bf16_f32 v142, v142, v143
	v_cvt_pk_bf16_f32 v143, v172, v173
	global_store_dwordx4 v[170:171], v[140:143], off
	s_nop 1
	v_mov_b32_e32 v140, v134
	v_mov_b32_e32 v141, v135
	v_mov_b32_e32 v134, v132
	v_mov_b32_e32 v135, v133
	v_cvt_pk_bf16_f32 v132, v136, v137
	v_cvt_pk_bf16_f32 v133, v138, v139
	v_cvt_pk_bf16_f32 v134, v134, v135
	v_cvt_pk_bf16_f32 v135, v140, v141
	global_store_dwordx4 v[170:171], v[132:135], off offset:256
	s_nop 1
	v_add_u32_e32 v132, s6, v162
	v_ashrrev_i32_e32 v133, 31, v132
	v_lshlrev_b64 v[132:133], 11, v[132:133]
	v_lshl_add_u64 v[132:133], s[10:11], 0, v[132:133]
	v_lshl_add_u64 v[132:133], v[132:133], 0, v[158:159]
	v_mov_b32_e32 v134, v126
	v_mov_b32_e32 v135, v127
	v_mov_b32_e32 v126, v124
	v_mov_b32_e32 v127, v125
	v_cvt_pk_bf16_f32 v124, v128, v129
	v_cvt_pk_bf16_f32 v125, v130, v131
	v_cvt_pk_bf16_f32 v126, v126, v127
	v_cvt_pk_bf16_f32 v127, v134, v135
	global_store_dwordx4 v[132:133], v[124:127], off
	s_nop 1
	v_mov_b32_e32 v124, v118
	v_mov_b32_e32 v125, v119
	v_mov_b32_e32 v118, v116
	v_mov_b32_e32 v119, v117
	v_cvt_pk_bf16_f32 v116, v120, v121
	v_cvt_pk_bf16_f32 v117, v122, v123
	v_cvt_pk_bf16_f32 v118, v118, v119
	v_cvt_pk_bf16_f32 v119, v124, v125
	global_store_dwordx4 v[132:133], v[116:119], off offset:256
	s_nop 1
	v_add_u32_e32 v116, s6, v163
	v_ashrrev_i32_e32 v117, 31, v116
	v_lshlrev_b64 v[116:117], 11, v[116:117]
	v_lshl_add_u64 v[116:117], s[10:11], 0, v[116:117]
	v_lshl_add_u64 v[116:117], v[116:117], 0, v[158:159]
	v_mov_b32_e32 v118, v94
	v_mov_b32_e32 v119, v95
	v_mov_b32_e32 v94, v92
	v_mov_b32_e32 v95, v93
	v_cvt_pk_bf16_f32 v92, v96, v97
	v_cvt_pk_bf16_f32 v93, v98, v99
	v_cvt_pk_bf16_f32 v94, v94, v95
	v_cvt_pk_bf16_f32 v95, v118, v119
	global_store_dwordx4 v[116:117], v[92:95], off
	s_nop 1
	v_mov_b32_e32 v92, v86
	v_mov_b32_e32 v93, v87
	v_mov_b32_e32 v86, v84
	v_mov_b32_e32 v87, v85
	v_cvt_pk_bf16_f32 v84, v88, v89
	v_cvt_pk_bf16_f32 v85, v90, v91
	v_cvt_pk_bf16_f32 v86, v86, v87
	v_cvt_pk_bf16_f32 v87, v92, v93
	global_store_dwordx4 v[116:117], v[84:87], off offset:256
	s_nop 1
	v_add_u32_e32 v84, s6, v164
	v_ashrrev_i32_e32 v85, 31, v84
	v_lshlrev_b64 v[84:85], 11, v[84:85]
	v_lshl_add_u64 v[84:85], s[10:11], 0, v[84:85]
	v_lshl_add_u64 v[84:85], v[84:85], 0, v[158:159]
	v_mov_b32_e32 v86, v78
	v_mov_b32_e32 v87, v79
	v_mov_b32_e32 v78, v76
	v_mov_b32_e32 v79, v77
	v_cvt_pk_bf16_f32 v76, v80, v81
	v_cvt_pk_bf16_f32 v77, v82, v83
	v_cvt_pk_bf16_f32 v78, v78, v79
	v_cvt_pk_bf16_f32 v79, v86, v87
	global_store_dwordx4 v[84:85], v[76:79], off
	s_nop 1
	v_mov_b32_e32 v76, v70
	v_mov_b32_e32 v77, v71
	v_mov_b32_e32 v70, v68
	v_mov_b32_e32 v71, v69
	v_cvt_pk_bf16_f32 v68, v72, v73
	v_cvt_pk_bf16_f32 v69, v74, v75
	v_cvt_pk_bf16_f32 v70, v70, v71
	v_cvt_pk_bf16_f32 v71, v76, v77
	global_store_dwordx4 v[84:85], v[68:71], off offset:256
	s_nop 1
	v_add_u32_e32 v68, s6, v165
	v_ashrrev_i32_e32 v69, 31, v68
	v_lshlrev_b64 v[68:69], 11, v[68:69]
	v_lshl_add_u64 v[68:69], s[10:11], 0, v[68:69]
	v_lshl_add_u64 v[68:69], v[68:69], 0, v[158:159]
	v_mov_b32_e32 v70, v62
	v_mov_b32_e32 v71, v63
	v_mov_b32_e32 v62, v60
	v_mov_b32_e32 v63, v61
	v_cvt_pk_bf16_f32 v60, v64, v65
	v_cvt_pk_bf16_f32 v61, v66, v67
	v_cvt_pk_bf16_f32 v62, v62, v63
	v_cvt_pk_bf16_f32 v63, v70, v71
	global_store_dwordx4 v[68:69], v[60:63], off
	s_nop 1
	v_mov_b32_e32 v60, v50
	v_mov_b32_e32 v61, v51
	v_mov_b32_e32 v50, v48
	v_mov_b32_e32 v51, v49
	v_cvt_pk_bf16_f32 v48, v56, v57
	v_cvt_pk_bf16_f32 v49, v58, v59
	s_nop 0
	v_cvt_pk_bf16_f32 v50, v50, v51
	v_cvt_pk_bf16_f32 v51, v60, v61
	global_store_dwordx4 v[68:69], v[48:51], off offset:256
	s_nop 1
	v_add_u32_e32 v48, s6, v166
	v_ashrrev_i32_e32 v49, 31, v48
	v_lshlrev_b64 v[48:49], 11, v[48:49]
	v_lshl_add_u64 v[48:49], s[10:11], 0, v[48:49]
	v_lshl_add_u64 v[48:49], v[48:49], 0, v[158:159]
	v_mov_b32_e32 v50, v54
	v_mov_b32_e32 v51, v55
	v_mov_b32_e32 v54, v46
	v_mov_b32_e32 v55, v47
	v_mov_b32_e32 v46, v44
	v_mov_b32_e32 v47, v45
	v_cvt_pk_bf16_f32 v44, v52, v53
	v_cvt_pk_bf16_f32 v45, v50, v51
	s_nop 0
	v_cvt_pk_bf16_f32 v46, v46, v47
	v_cvt_pk_bf16_f32 v47, v54, v55
	global_store_dwordx4 v[48:49], v[44:47], off
	s_nop 1
	v_mov_b32_e32 v44, v34
	v_mov_b32_e32 v45, v35
	v_mov_b32_e32 v34, v32
	v_mov_b32_e32 v35, v33
	v_cvt_pk_bf16_f32 v32, v40, v41
	v_cvt_pk_bf16_f32 v33, v42, v43
	s_nop 0
	v_cvt_pk_bf16_f32 v34, v34, v35
	v_cvt_pk_bf16_f32 v35, v44, v45
	global_store_dwordx4 v[48:49], v[32:35], off offset:256
	s_nop 1
	v_add_u32_e32 v32, s6, v167
	v_ashrrev_i32_e32 v33, 31, v32
	v_lshlrev_b64 v[32:33], 11, v[32:33]
	v_lshl_add_u64 v[32:33], s[10:11], 0, v[32:33]
	v_lshl_add_u64 v[32:33], v[32:33], 0, v[158:159]
	v_mov_b32_e32 v34, v38
	v_mov_b32_e32 v35, v39
	v_mov_b32_e32 v38, v30
	v_mov_b32_e32 v39, v31
	v_mov_b32_e32 v30, v28
	v_mov_b32_e32 v31, v29
	v_cvt_pk_bf16_f32 v28, v36, v37
	v_cvt_pk_bf16_f32 v29, v34, v35
	s_nop 0
	v_cvt_pk_bf16_f32 v30, v30, v31
	v_cvt_pk_bf16_f32 v31, v38, v39
	global_store_dwordx4 v[32:33], v[28:31], off
	s_nop 1
	v_mov_b32_e32 v28, v18
	v_mov_b32_e32 v29, v19
	v_mov_b32_e32 v18, v16
	v_mov_b32_e32 v19, v17
	v_cvt_pk_bf16_f32 v16, v24, v25
	v_cvt_pk_bf16_f32 v17, v26, v27
	s_nop 0
	v_cvt_pk_bf16_f32 v18, v18, v19
	v_cvt_pk_bf16_f32 v19, v28, v29
	global_store_dwordx4 v[32:33], v[16:19], off offset:256
	s_nop 1
	v_add_u32_e32 v16, s6, v168
	v_ashrrev_i32_e32 v17, 31, v16
	v_lshlrev_b64 v[16:17], 11, v[16:17]
	v_lshl_add_u64 v[16:17], s[10:11], 0, v[16:17]
	v_lshl_add_u64 v[16:17], v[16:17], 0, v[158:159]
	v_mov_b32_e32 v18, v22
	v_mov_b32_e32 v19, v23
	v_mov_b32_e32 v22, v14
	v_mov_b32_e32 v23, v15
	v_mov_b32_e32 v14, v12
	v_mov_b32_e32 v15, v13
	v_cvt_pk_bf16_f32 v12, v20, v21
	v_cvt_pk_bf16_f32 v13, v18, v19
	s_nop 0
	v_cvt_pk_bf16_f32 v14, v14, v15
	v_cvt_pk_bf16_f32 v15, v22, v23
	global_store_dwordx4 v[16:17], v[12:15], off
	s_nop 1
	v_mov_b32_e32 v12, v6
	v_mov_b32_e32 v13, v7
	v_mov_b32_e32 v6, v4
	v_mov_b32_e32 v7, v5
	v_cvt_pk_bf16_f32 v4, v8, v9
	v_cvt_pk_bf16_f32 v5, v10, v11
	s_nop 0
	v_cvt_pk_bf16_f32 v6, v6, v7
	v_cvt_pk_bf16_f32 v7, v12, v13
	global_store_dwordx4 v[16:17], v[4:7], off offset:256
	s_cbranch_vccnz .LBB0_1812
	s_branch .LBB0_1811
